# expert-up padded-row MFMA skip with the flag compare moved ahead of the barrier (1)
# speedup vs baseline: 1.0073x; 1.0073x over previous
; #define PG8_STAGE(bufoff, gbase, voff) do { _Pragma("unroll") for (int _i = 0; _i < 2; ++_i) \
;         __builtin_amdgcn_global_load_lds((const unsigned*)((const char*)(gbase) + (voff)[_i]), (LAS unsigned*)(lds + (bufoff) + ldsw + _i * 8192), 16, 0, 0); } while (0)
; #define PG8_LDA(dst, b, h) do { _Pragma("unroll") for (int m = 0; m < 4; ++m) dst[m] = PG8_LD8(lds + PG8_SA(b, h) + aoff + m * 2048); } while (0)
; #define PG8_LDB(dst, b, h) do { _Pragma("unroll") for (int n = 0; n < 2; ++n) dst[n] = PG8_LD8(lds + PG8_SB(b, h) + boff + n * 2048); } while (0)
; #define PG8_WAIT_V(n) asm volatile("s_waitcnt vmcnt(" #n ")" ::: "memory")
; #define PG8_WAIT_L(n) asm volatile("s_waitcnt lgkmcnt(" #n ")" ::: "memory")
; #define PG8_BAR __builtin_amdgcn_s_barrier()
; #define PG8_SCHED __builtin_amdgcn_sched_barrier(0)
;     ...
;             PG8_LDB(B0, 0, 0); PG8_LDB(B1, 0, 1); PG8_SCHED; PG8_LDA(At, 0, 0); PG8_STAGE(PG8_SA(1, 1), a1 + hstep, voffA);
;             PG8_WAIT_V(8); PG8_WAIT_L(0); PG8_BAR; PG8_MMA(0, 0, At, B0); PG8_MMA(0, 1, At, B1); PG8_BAR; PG8_SCHED;
;             PG8_LDA(At, 0, 1); PG8_STAGE(PG8_SB(0, 0), b2, voffB); PG8_STAGE(PG8_SB(0, 1), b2 + hstep, voffB); PG8_STAGE(PG8_SA(0, 0), a2, voffA);
;             PG8_WAIT_V(8); PG8_WAIT_L(0); PG8_BAR; PG8_MMA(1, 0, At, B0); PG8_MMA(1, 1, At, B1); PG8_BAR; PG8_SCHED;
.LBB0_2259:
	ds_read_b128 v[18:21], v166
	ds_read_b128 v[22:25], v166 offset:1024
	ds_read_b128 v[26:29], v166 offset:2048
	ds_read_b128 v[30:33], v166 offset:3072
	ds_read_b128 v[2:5], v190
	ds_read_b128 v[6:9], v190 offset:1024
	ds_read_b128 v[10:13], v190 offset:2048
	ds_read_b128 v[14:17], v190 offset:3072
	s_add_i32 s39, s41, 2
	s_add_u32 s66, s64, 0x80
	s_addc_u32 s67, s65, 0
	s_cmp_eq_u32 s63, s41
	s_cselect_b64 vcc, -1, 0
	s_cselect_b32 s67, s47, s67
	s_cselect_b32 s66, s46, s66
	v_cndmask_b32_e32 v185, v175, v173, vcc
	v_cndmask_b32_e32 v184, v174, v172, vcc
	v_lshl_add_u64 v[186:187], s[64:65], 0, v[168:169]
	s_add_i32 m0, s44, 0xc000
	ds_read_b128 v[176:179], v191
	ds_read_b128 v[180:183], v191 offset:1024
	ds_read_b128 v[196:199], v191 offset:2048
	ds_read_b128 v[200:203], v191 offset:3072
	ds_read_b128 v[204:207], v191 offset:4096
	ds_read_b128 v[208:211], v191 offset:5120
	ds_read_b128 v[212:215], v191 offset:6144
	ds_read_b128 v[216:219], v191 offset:7168
	global_load_lds_dwordx4 v[186:187], off
	v_lshl_add_u64 v[186:187], s[64:65], 0, v[170:171]
	s_add_i32 m0, s44, 0xe000
	s_nop 0
	global_load_lds_dwordx4 v[186:187], off
	v_cmp_eq_f32_e32 vcc, 0, v252
	s_waitcnt vmcnt(8)
	s_waitcnt lgkmcnt(0)
	s_barrier
	s_cbranch_vccnz .Lp21sk_0
	s_setprio 1
	s_waitcnt lgkmcnt(0)
	v_mfma_f32_16x16x128_f8f6f4 v[158:161], v[18:25], v[176:183], v[158:161]
	v_mfma_f32_16x16x128_f8f6f4 v[154:157], v[26:33], v[176:183], v[154:157]
	v_mfma_f32_16x16x128_f8f6f4 v[142:145], v[18:25], v[196:203], v[142:145]
	v_mfma_f32_16x16x128_f8f6f4 v[138:141], v[26:33], v[196:203], v[138:141]
	v_mfma_f32_16x16x128_f8f6f4 v[126:129], v[18:25], v[204:211], v[126:129]
	v_mfma_f32_16x16x128_f8f6f4 v[122:125], v[26:33], v[204:211], v[122:125]
	v_mfma_f32_16x16x128_f8f6f4 v[110:113], v[18:25], v[212:219], v[110:113]
	v_mfma_f32_16x16x128_f8f6f4 v[106:109], v[26:33], v[212:219], v[106:109]
	s_nop 7
	s_setprio 0
	s_setprio 1
	v_mfma_f32_16x16x128_f8f6f4 v[146:149], v[2:9], v[176:183], v[146:149]
	v_mfma_f32_16x16x128_f8f6f4 v[150:153], v[10:17], v[176:183], v[150:153]
	v_mfma_f32_16x16x128_f8f6f4 v[130:133], v[2:9], v[196:203], v[130:133]
	v_mfma_f32_16x16x128_f8f6f4 v[134:137], v[10:17], v[196:203], v[134:137]
	v_mfma_f32_16x16x128_f8f6f4 v[114:117], v[2:9], v[204:211], v[114:117]
	v_mfma_f32_16x16x128_f8f6f4 v[118:121], v[10:17], v[204:211], v[118:121]
	v_mfma_f32_16x16x128_f8f6f4 v[98:101], v[2:9], v[212:219], v[98:101]
	v_mfma_f32_16x16x128_f8f6f4 v[102:105], v[10:17], v[212:219], v[102:105]
	s_nop 7
	s_setprio 0
.Lp21sk_0:
	s_barrier
	s_add_i32 s41, s69, s34
	v_lshl_add_u64 v[176:177], v[184:185], 0, v[162:163]
	s_mov_b32 m0, s41
	ds_read_b128 v[196:199], v191 offset:16384
	ds_read_b128 v[200:203], v191 offset:17408
	ds_read_b128 v[204:207], v191 offset:18432
	ds_read_b128 v[208:211], v191 offset:19456
	ds_read_b128 v[212:215], v191 offset:20480
	ds_read_b128 v[216:219], v191 offset:21504
	ds_read_b128 v[220:223], v191 offset:22528
	ds_read_b128 v[224:227], v191 offset:23552
	global_load_lds_dwordx4 v[176:177], off
	v_lshl_add_u64 v[178:179], v[184:185], 0, v[164:165]
	s_add_i32 m0, s41, 0x2000
	v_lshl_add_u64 v[182:183], v[184:185], 0, s[20:21]
	s_add_i32 s41, s70, s34
	global_load_lds_dwordx4 v[178:179], off
	v_lshl_add_u64 v[180:181], v[182:183], 0, v[162:163]
	s_mov_b32 m0, s41
	v_lshl_add_u64 v[182:183], v[182:183], 0, v[164:165]
	global_load_lds_dwordx4 v[180:181], off
	s_add_i32 m0, s41, 0x2000
	v_lshl_add_u64 v[184:185], s[66:67], 0, v[162:163]
	global_load_lds_dwordx4 v[182:183], off
	s_mov_b32 m0, s44
	v_lshl_add_u64 v[186:187], s[66:67], 0, v[164:165]
	global_load_lds_dwordx4 v[184:185], off
	s_mov_b32 m0, s45
	s_nop 0
	global_load_lds_dwordx4 v[186:187], off
	v_cmp_eq_f32_e32 vcc, 0, v253
	s_waitcnt vmcnt(8)
	s_waitcnt lgkmcnt(0)
	s_barrier
	s_cbranch_vccnz .Lp21sk_1
	s_setprio 1
	s_waitcnt lgkmcnt(0)
	v_mfma_f32_16x16x128_f8f6f4 v[94:97], v[18:25], v[196:203], v[94:97]
	v_mfma_f32_16x16x128_f8f6f4 v[90:93], v[26:33], v[196:203], v[90:93]
	v_mfma_f32_16x16x128_f8f6f4 v[78:81], v[18:25], v[204:211], v[78:81]
	v_mfma_f32_16x16x128_f8f6f4 v[74:77], v[26:33], v[204:211], v[74:77]
	v_mfma_f32_16x16x128_f8f6f4 v[62:65], v[18:25], v[212:219], v[62:65]
	v_mfma_f32_16x16x128_f8f6f4 v[58:61], v[26:33], v[212:219], v[58:61]
	v_mfma_f32_16x16x128_f8f6f4 v[46:49], v[18:25], v[220:227], v[46:49]
	v_mfma_f32_16x16x128_f8f6f4 v[42:45], v[26:33], v[220:227], v[42:45]
	s_nop 7
	s_setprio 0
	s_setprio 1
	v_mfma_f32_16x16x128_f8f6f4 v[82:85], v[2:9], v[196:203], v[82:85]
	v_mfma_f32_16x16x128_f8f6f4 v[86:89], v[10:17], v[196:203], v[86:89]
	v_mfma_f32_16x16x128_f8f6f4 v[66:69], v[2:9], v[204:211], v[66:69]
	v_mfma_f32_16x16x128_f8f6f4 v[70:73], v[10:17], v[204:211], v[70:73]
	v_mfma_f32_16x16x128_f8f6f4 v[50:53], v[2:9], v[212:219], v[50:53]
	v_mfma_f32_16x16x128_f8f6f4 v[54:57], v[10:17], v[212:219], v[54:57]
	v_mfma_f32_16x16x128_f8f6f4 v[34:37], v[2:9], v[220:227], v[34:37]
	v_mfma_f32_16x16x128_f8f6f4 v[38:41], v[10:17], v[220:227], v[38:41]
	s_nop 7
	s_setprio 0
; #define PG8_STAGE(bufoff, gbase, voff) do { _Pragma("unroll") for (int _i = 0; _i < 2; ++_i) \
;         __builtin_amdgcn_global_load_lds((const unsigned*)((const char*)(gbase) + (voff)[_i]), (LAS unsigned*)(lds + (bufoff) + ldsw + _i * 8192), 16, 0, 0); } while (0)
; #define PG8_LDA(dst, b, h) do { _Pragma("unroll") for (int m = 0; m < 4; ++m) dst[m] = PG8_LD8(lds + PG8_SA(b, h) + aoff + m * 2048); } while (0)
; #define PG8_LDB(dst, b, h) do { _Pragma("unroll") for (int n = 0; n < 2; ++n) dst[n] = PG8_LD8(lds + PG8_SB(b, h) + boff + n * 2048); } while (0)
; #define PG8_WAIT_V(n) asm volatile("s_waitcnt vmcnt(" #n ")" ::: "memory")
; #define PG8_WAIT_L(n) asm volatile("s_waitcnt lgkmcnt(" #n ")" ::: "memory")
; #define PG8_BAR __builtin_amdgcn_s_barrier()
; #define PG8_SCHED __builtin_amdgcn_sched_barrier(0)
;     ...
;             PG8_LDB(B0, 1, 0); PG8_LDB(B1, 1, 1); PG8_SCHED; PG8_LDA(At, 1, 0); PG8_STAGE(PG8_SA(0, 1), a2 + hstep, voffA);
;             PG8_WAIT_V(8); PG8_WAIT_L(0); PG8_BAR; PG8_MMA(0, 0, At, B0); PG8_MMA(0, 1, At, B1); PG8_BAR; PG8_SCHED;
;             PG8_LDA(At, 1, 1); PG8_STAGE(PG8_SB(1, 0), b3, voffB); PG8_STAGE(PG8_SB(1, 1), b3 + hstep, voffB); PG8_STAGE(PG8_SA(1, 0), a3, voffA);
;             PG8_WAIT_V(8); PG8_WAIT_L(0); PG8_BAR; PG8_MMA(1, 0, At, B0); PG8_MMA(1, 1, At, B1); PG8_BAR; PG8_SCHED;
.Lp21sk_1:
	s_barrier
	s_add_i32 s41, 0, 0x18000
	s_add_i32 s72, 0, 0x1c000
	v_add_u32_e32 v14, s41, v188
	v_add_u32_e32 v30, s72, v188
	ds_read_b128 v[2:5], v14
	ds_read_b128 v[6:9], v14 offset:1024
	ds_read_b128 v[10:13], v14 offset:2048
	ds_read_b128 v[14:17], v14 offset:3072
	ds_read_b128 v[18:21], v30
	ds_read_b128 v[22:25], v30 offset:1024
	ds_read_b128 v[26:29], v30 offset:2048
	ds_read_b128 v[30:33], v30 offset:3072
	s_add_u32 s66, s66, s20
	s_addc_u32 s67, s67, s21
	s_mov_b32 m0, s49
	v_lshl_add_u64 v[192:193], s[66:67], 0, v[162:163]
	ds_read_b128 v[196:199], v191 offset:32768
	ds_read_b128 v[200:203], v191 offset:33792
	ds_read_b128 v[204:207], v191 offset:34816
	ds_read_b128 v[208:211], v191 offset:35840
	ds_read_b128 v[212:215], v191 offset:36864
	ds_read_b128 v[216:219], v191 offset:37888
	ds_read_b128 v[220:223], v191 offset:38912
	ds_read_b128 v[224:227], v191 offset:39936
	global_load_lds_dwordx4 v[192:193], off
	v_lshl_add_u64 v[192:193], s[66:67], 0, v[164:165]
	s_mov_b32 m0, s50
	s_nop 0
	global_load_lds_dwordx4 v[192:193], off
	v_cmp_eq_f32_e32 vcc, 0, v252
	s_waitcnt vmcnt(8)
	s_waitcnt lgkmcnt(0)
	s_barrier
	s_cbranch_vccnz .Lp21sk_2
	s_setprio 1
	s_waitcnt lgkmcnt(0)
	v_mfma_f32_16x16x128_f8f6f4 v[158:161], v[2:9], v[196:203], v[158:161]
	v_mfma_f32_16x16x128_f8f6f4 v[154:157], v[10:17], v[196:203], v[154:157]
	v_mfma_f32_16x16x128_f8f6f4 v[142:145], v[2:9], v[204:211], v[142:145]
	v_mfma_f32_16x16x128_f8f6f4 v[138:141], v[10:17], v[204:211], v[138:141]
	v_mfma_f32_16x16x128_f8f6f4 v[126:129], v[2:9], v[212:219], v[126:129]
	v_mfma_f32_16x16x128_f8f6f4 v[122:125], v[10:17], v[212:219], v[122:125]
	v_mfma_f32_16x16x128_f8f6f4 v[110:113], v[2:9], v[220:227], v[110:113]
	v_mfma_f32_16x16x128_f8f6f4 v[106:109], v[10:17], v[220:227], v[106:109]
	s_nop 7
	s_setprio 0
	s_setprio 1
	v_mfma_f32_16x16x128_f8f6f4 v[146:149], v[18:25], v[196:203], v[146:149]
	v_mfma_f32_16x16x128_f8f6f4 v[150:153], v[26:33], v[196:203], v[150:153]
	v_mfma_f32_16x16x128_f8f6f4 v[130:133], v[18:25], v[204:211], v[130:133]
	v_mfma_f32_16x16x128_f8f6f4 v[134:137], v[26:33], v[204:211], v[134:137]
	v_mfma_f32_16x16x128_f8f6f4 v[114:117], v[18:25], v[212:219], v[114:117]
	v_mfma_f32_16x16x128_f8f6f4 v[118:121], v[26:33], v[212:219], v[118:121]
	v_mfma_f32_16x16x128_f8f6f4 v[98:101], v[18:25], v[220:227], v[98:101]
	v_mfma_f32_16x16x128_f8f6f4 v[102:105], v[26:33], v[220:227], v[102:105]
	s_nop 7
	s_setprio 0
.Lp21sk_2:
	s_barrier
	s_add_i32 s41, s41, s34
	v_lshl_add_u64 v[176:177], v[176:177], 0, s[24:25]
	s_mov_b32 m0, s41
	ds_read_b128 v[196:199], v191 offset:49152
	ds_read_b128 v[200:203], v191 offset:50176
	ds_read_b128 v[204:207], v191 offset:51200
	ds_read_b128 v[208:211], v191 offset:52224
	ds_read_b128 v[212:215], v191 offset:53248
	ds_read_b128 v[216:219], v191 offset:54272
	ds_read_b128 v[220:223], v191 offset:55296
	ds_read_b128 v[224:227], v191 offset:56320
	global_load_lds_dwordx4 v[176:177], off
	v_lshl_add_u64 v[176:177], v[178:179], 0, s[24:25]
	s_add_i32 m0, s41, 0x2000
	s_add_i32 s41, s72, s34
	global_load_lds_dwordx4 v[176:177], off
	v_lshl_add_u64 v[176:177], v[180:181], 0, s[24:25]
	s_mov_b32 m0, s41
	s_nop 0
	global_load_lds_dwordx4 v[176:177], off
	v_lshl_add_u64 v[176:177], v[182:183], 0, s[24:25]
	s_add_i32 m0, s41, 0x2000
	s_nop 0
	global_load_lds_dwordx4 v[176:177], off
	v_lshl_add_u64 v[176:177], v[184:185], 0, s[24:25]
	s_mov_b32 m0, s56
	s_nop 0
	global_load_lds_dwordx4 v[176:177], off
	v_lshl_add_u64 v[176:177], v[186:187], 0, s[24:25]
	s_mov_b32 m0, s57
	s_nop 0
	global_load_lds_dwordx4 v[176:177], off
	v_cmp_eq_f32_e32 vcc, 0, v253
	s_waitcnt vmcnt(8)
	s_waitcnt lgkmcnt(0)
	s_barrier
	s_cbranch_vccnz .Lp21sk_3
	s_setprio 1
	s_waitcnt lgkmcnt(0)
	v_mfma_f32_16x16x128_f8f6f4 v[94:97], v[2:9], v[196:203], v[94:97]
	v_mfma_f32_16x16x128_f8f6f4 v[90:93], v[10:17], v[196:203], v[90:93]
	v_mfma_f32_16x16x128_f8f6f4 v[78:81], v[2:9], v[204:211], v[78:81]
	v_mfma_f32_16x16x128_f8f6f4 v[74:77], v[10:17], v[204:211], v[74:77]
	v_mfma_f32_16x16x128_f8f6f4 v[62:65], v[2:9], v[212:219], v[62:65]
	v_mfma_f32_16x16x128_f8f6f4 v[58:61], v[10:17], v[212:219], v[58:61]
	v_mfma_f32_16x16x128_f8f6f4 v[46:49], v[2:9], v[220:227], v[46:49]
	v_mfma_f32_16x16x128_f8f6f4 v[42:45], v[10:17], v[220:227], v[42:45]
	s_nop 7
	s_setprio 0
	s_setprio 1
	v_mfma_f32_16x16x128_f8f6f4 v[82:85], v[18:25], v[196:203], v[82:85]
	v_mfma_f32_16x16x128_f8f6f4 v[86:89], v[26:33], v[196:203], v[86:89]
	v_mfma_f32_16x16x128_f8f6f4 v[66:69], v[18:25], v[204:211], v[66:69]
	v_mfma_f32_16x16x128_f8f6f4 v[70:73], v[26:33], v[204:211], v[70:73]
	v_mfma_f32_16x16x128_f8f6f4 v[50:53], v[18:25], v[212:219], v[50:53]
	v_mfma_f32_16x16x128_f8f6f4 v[54:57], v[26:33], v[212:219], v[54:57]
	v_mfma_f32_16x16x128_f8f6f4 v[34:37], v[18:25], v[220:227], v[34:37]
	v_mfma_f32_16x16x128_f8f6f4 v[38:41], v[26:33], v[220:227], v[38:41]
	s_nop 7
	s_setprio 0
